# lru_a: one (b,kb) quarter of 132 tiles per workgroup instead of 3 rounds of 48-tile tasks (balanced, single task prologue)
# speedup vs baseline: 1.0045x; 1.0045x over previous
; __device__ __forceinline__ void ph_lru_a(const Frame& F, int jj) {
;     ...
;         const int nt0 = grp * 48;
;         LruRaw raw; lru_load(F, b, kb, nt0 + F.wave, raw);
;         for (int ti = F.wave; ti < 48; ti += 8) {
;             const int nt = nt0 + ti;
;             float av[2][4][4], xv[2][4][4]; unsigned pw[2][4][4];
;             lru_conv(F, raw, CT, ucb);
;             lru_load(F, b, kb, nt0 + min(ti + 8, 40 + F.wave), raw);
.LBB0_88:
	s_add_u32 s82, s62, 0x1b2d8000
	v_writelane_b32 v250, s28, 5
	s_addc_u32 s83, s63, 0
	s_add_u32 s0, s62, 0xda98000
	v_writelane_b32 v250, s29, 6
	v_writelane_b32 v250, s0, 7
	s_addc_u32 s0, s63, 0
	s_cmpk_lt_i32 s89, 0x35d0
	v_writelane_b32 v250, s0, 8
	s_cselect_b64 s[0:1], -1, 0
	v_writelane_b32 v250, s0, 9
	s_lshl_b32 s19, s3, 2
	s_movk_i32 s16, 0xa00
	v_writelane_b32 v250, s1, 10
	s_lshl_b32 s0, s3, 1
	v_writelane_b32 v250, s0, 11
	s_add_u32 s0, s62, 0x200
	s_addc_u32 s1, s63, 0
	v_writelane_b32 v250, s0, 12
	s_mov_b32 s65, 0
	s_mul_i32 s81, s3, 24
	v_writelane_b32 v250, s1, 13
	s_add_u32 s0, s62, 0x1000
	s_addc_u32 s1, s63, 0
	v_writelane_b32 v250, s0, 14
	v_mov_b32_e32 v174, 1
	v_mov_b32_e32 v175, 0x358637bd
	v_writelane_b32 v250, s1, 15
	s_add_u32 s0, s62, 0x1100
	s_addc_u32 s1, s63, 0
	v_writelane_b32 v250, s0, 16
	v_mov_b32_e32 v176, 0x3727c5ac
	v_mbcnt_hi_u32_b32 v177, -1, v1
	v_writelane_b32 v250, s1, 17
	s_add_u32 s0, s62, 0x1200
	s_addc_u32 s1, s63, 0
	v_writelane_b32 v250, s0, 18
	v_mov_b32_e32 v178, 0x3e38aa3b
	v_mov_b32_e32 v144, 0x3f317218
	v_writelane_b32 v250, s1, 19
	s_add_u32 s0, s62, 0x1300
	s_addc_u32 s1, s63, 0
	v_writelane_b32 v250, s0, 20
	s_cmp_eq_u32 s26, 15
	v_mov_b32_e32 v179, 0x41b17218
	v_writelane_b32 v250, s1, 21
	s_cselect_b64 s[0:1], -1, 0
	v_writelane_b32 v250, s0, 22
	s_cmp_eq_u32 s26, 14
	v_mov_b32_e32 v180, 0x42a00000
	v_writelane_b32 v250, s1, 23
	s_cselect_b64 s[0:1], -1, 0
	v_writelane_b32 v250, s0, 24
	s_cmp_eq_u32 s26, 13
	v_mov_b32_e32 v181, 0x201
	v_writelane_b32 v250, s1, 25
	s_cselect_b64 s[0:1], -1, 0
	v_writelane_b32 v250, s0, 26
	s_cmp_eq_u32 s26, 12
	v_mov_b32_e32 v186, 0x1ff
	v_writelane_b32 v250, s1, 27
	s_cselect_b64 s[0:1], -1, 0
	v_writelane_b32 v250, s0, 28
	s_cmp_eq_u32 s26, 11
	v_not_b32_e32 v187, 16
	v_writelane_b32 v250, s1, 29
	s_cselect_b64 s[0:1], -1, 0
	v_writelane_b32 v250, s0, 30
	s_cmp_eq_u32 s26, 10
	v_mov_b32_e32 v188, 0xf149f2ca
	v_writelane_b32 v250, s1, 31
	s_cselect_b64 s[0:1], -1, 0
	v_writelane_b32 v250, s0, 32
	s_cmp_eq_u32 s26, 9
	v_mov_b32_e32 v189, 0x43dc0000
	v_writelane_b32 v250, s1, 33
	s_cselect_b64 s[0:1], -1, 0
	v_writelane_b32 v250, s0, 34
	s_cmp_eq_u32 s26, 8
	s_mov_b32 s39, 0x8000
	v_writelane_b32 v250, s1, 35
	s_cselect_b64 s[0:1], -1, 0
	v_writelane_b32 v250, s0, 36
	s_cmp_eq_u32 s26, 7
	s_movk_i32 s97, 0x1000
	v_writelane_b32 v250, s1, 37
	s_cselect_b64 s[0:1], -1, 0
	v_writelane_b32 v250, s0, 38
	s_cmp_eq_u32 s26, 6
	s_movk_i32 s73, 0x3000
	v_writelane_b32 v250, s1, 39
	s_cselect_b64 s[0:1], -1, 0
	v_writelane_b32 v250, s0, 40
	s_cmp_eq_u32 s26, 5
	s_movk_i32 s88, 0x2000
	v_writelane_b32 v250, s1, 41
	s_cselect_b64 s[0:1], -1, 0
	v_writelane_b32 v250, s0, 42
	s_cmp_eq_u32 s26, 4
	s_mov_b32 s90, 0x7f800000
	v_writelane_b32 v250, s1, 43
	s_cselect_b64 s[0:1], -1, 0
	v_writelane_b32 v250, s0, 44
	s_cmp_eq_u32 s26, 3
	s_mov_b32 s91, 0xffff0000
	v_writelane_b32 v250, s1, 45
	s_cselect_b64 s[0:1], -1, 0
	v_writelane_b32 v250, s0, 46
	s_cmp_eq_u32 s26, 2
	s_mov_b32 s92, 0x800000
	v_writelane_b32 v250, s1, 47
	s_cselect_b64 s[0:1], -1, 0
	v_writelane_b32 v250, s0, 48
	s_cmp_eq_u32 s26, 1
	s_mov_b32 s93, 0x3f317217
	v_writelane_b32 v250, s1, 49
	s_cselect_b64 s[0:1], -1, 0
	v_writelane_b32 v250, s0, 50
	s_cmp_eq_u32 s26, 0
	s_mov_b32 s94, 0xc2a00000
	v_writelane_b32 v250, s1, 51
	s_cselect_b64 s[0:1], -1, 0
	v_writelane_b32 v250, s0, 52
	s_mov_b32 s95, 0xc3dc0000
	s_mov_b32 s78, 0x3fd744fd
	v_writelane_b32 v250, s1, 53
	s_lshl_b32 s0, s26, 8
	s_add_u32 s0, s62, s0
	s_addc_u32 s1, s63, 0
	s_add_u32 s4, s0, 0x1400
	s_addc_u32 s5, s1, 0
	v_writelane_b32 v250, s4, 54
	s_add_u32 s0, s0, 0x2400
	s_addc_u32 s1, s1, 0
	v_writelane_b32 v250, s5, 55
	v_writelane_b32 v250, s0, 56
	s_mov_b32 s74, 0x41800000
	s_mov_b32 s72, 0x3d800000
	v_writelane_b32 v250, s1, 57
	s_add_u32 s0, s62, 0x3400
	s_addc_u32 s1, s63, 0
	v_writelane_b32 v250, s0, 58
	s_nop 1
	v_writelane_b32 v250, s1, 59
	s_add_u32 s0, s62, 0x3500
	s_addc_u32 s1, s63, 0
	v_writelane_b32 v250, s0, 60
	s_ashr_i32 s68, s89, 31
	s_nop 0
	v_writelane_b32 v250, s1, 61
	s_lshr_b32 s0, s68, 29
	s_add_i32 s0, s89, s0
	s_ashr_i32 s1, s0, 3
	s_and_b32 s0, s0, -8
	s_sub_i32 s0, s89, s0
	v_writelane_b32 v250, s1, 62
	s_cmp_lt_i32 s0, 0
	v_writelane_b32 v250, s0, 63
	s_cselect_b64 s[0:1], -1, 0
	v_writelane_b32 v251, s0, 0
	s_ashr_i32 s18, s3, 31
	s_nop 0
	v_writelane_b32 v251, s1, 1
	s_mul_i32 s0, s75, 0x1100
	s_add_i32 s17, s0, 0
	s_add_u32 s0, s62, 0x236d8000
	v_writelane_b32 v251, s0, 2
	s_addc_u32 s0, s63, 0
	v_writelane_b32 v251, s0, 3
	s_add_u32 s0, s62, 0x26858000
	s_addc_u32 s1, s63, 0
	v_writelane_b32 v251, s0, 4
	s_cmpk_lt_i32 s89, 0x2c0
	s_nop 0
	v_writelane_b32 v251, s1, 5
	s_cselect_b64 s[0:1], -1, 0
	v_writelane_b32 v251, s0, 6
	s_cmpk_lt_u32 s2, 0xc00
	s_nop 0
	v_writelane_b32 v251, s1, 7
	s_cselect_b64 s[0:1], -1, 0
	s_lshr_b32 s100, s75, 2
	s_lshl_b32 s100, s100, 3
	s_sub_i32 s100, s75, s100
	s_addk_i32 s100, 0x80
	s_add_i32 s33, s75, 40
	s_cmpk_eq_i32 s3, 0x100
	s_cselect_b32 s33, s100, s33
	v_writelane_b32 v251, s0, 8
	s_cmp_gt_i32 s89, 7
	s_nop 0
	v_writelane_b32 v251, s1, 9
	s_cselect_b64 s[0:1], -1, 0
	s_cmp_lt_i32 s3, 17
	s_cselect_b64 s[4:5], -1, 0
	s_or_b64 s[0:1], s[0:1], s[4:5]
	v_writelane_b32 v251, s0, 10
	s_nop 1
	v_writelane_b32 v251, s1, 11
	s_add_i32 s0, s89, -8
	s_add_i32 s1, s3, -8
	s_cmp_gt_i32 s3, 16
	s_cselect_b32 s4, s1, s3
	s_cselect_b32 s6, s0, s89
	s_and_b32 s0, s6, 7
	s_ashr_i32 s1, s4, 3
	s_mul_i32 s7, s0, s1
	s_ashr_i32 s0, s6, 3
	s_add_i32 s7, s7, s0
	s_lshl_b32 s0, s75, 4
	s_and_b32 s21, s0, 48
	s_lshr_b32 s0, s2, 7
	s_and_b32 s0, s0, 0x1fffffe
	s_and_b32 s8, s4, 7
; #define LAS __attribute__((address_space(3)))
; __device__ __forceinline__ Frame fresh(const Frame& F0) { Frame F = F0; int ln = lane_id_(); asm volatile("" : "+v"(ln)); F.lane = ln; F.tid = F0.wave * 64 + ln; return F; }
; #define SEAM(k) do { if (IN(k) && IN((k) + 1)) { xcd_barrier(bar); if (REPM & 1) xcd_barrier(bar); } } while (0)
; __global__ void __launch_bounds__(512, 2) mk_fwd(Args args) {
;     ...
;     { const int t0 = threadIdx.x; F.wave = __builtin_amdgcn_readfirstlane(t0 >> 6); F.lane = t0 & 63; F.tid = t0; } F.G = gridDim.x; F.wg = blockIdx.x;
;     F.mods = (float*)(args.ws + OFF_MODS); F.X = (float*)(args.ws + OFF_X); F.HB = (bf16_t*)(args.ws + OFF_HB); F.MIX = F.HB;
;     F.WB = args.ws + OFF_WB; F.R1 = args.ws + OFF_R1;
;     volatile LAS unsigned* xbw = (volatile LAS unsigned*)(F.lds + LDS_MISC);
;     if (F.tid < 4) xbw[F.tid] = 0u;
;     if (F.tid < 30) ((LAS unsigned long long*)(F.lds + LDS_MISC + MISC_INP))[F.tid] = (unsigned long long)args.in[F.tid];
;     __syncthreads();
;     const int lo = args.ph_lo, hi = args.ph_hi;
;     XcdBarrier bar; bar.bar = (unsigned*)(args.ws + OFF_CTL); bar.x = 0; bar.st = xbw;
;     if (hi - lo > 1) bar = xcd_barrier_post((unsigned*)(args.ws + OFF_CTL), xbw);
;     ...
;     if ((PHM & 1) && IN(0)) { ph_mods(fresh(F)); if (REPM & 65536) { __syncthreads(); ph_mods(fresh(F)); } } SEAM(0);
;     if ((PHM & 2) && IN(1)) { ph_init_x(fresh(F)); if (REPM & 131072) ph_init_x(fresh(F)); }
;     for (int l = 0; l < 4; ++l) {
;         const int pb = 2 + l * 10, j = l >> 1; const bool even = (l & 1) == 0;
;         float* mods_l = F.mods + (size_t)l * 5 * 6144;
;         F.WB = args.ws + OFF_WB + (size_t)(l & 1) * WB_END;
	s_lshl_b32 s23, s75, 5
	v_writelane_b32 v251, s0, 12
	s_add_u32 s0, s62, 0x2fcd8000
	s_addc_u32 s1, s63, 0
	v_writelane_b32 v251, s4, 13
	s_add_u32 s26, s62, 0x2bad8000
	v_writelane_b32 v251, s0, 14
	s_addc_u32 s27, s63, 0
	s_lshl_b32 s5, s75, 12
	v_writelane_b32 v251, s1, 15
	s_lshl_b32 s4, s89, 2
	s_bfe_u32 s0, s2, 0x20006
	s_add_i32 s9, s5, 0
	s_or_b32 s1, s0, s4
	v_writelane_b32 v251, s5, 16
	s_add_i32 s5, s9, 0x8000
	s_lshl_b32 s0, s1, 6
	v_writelane_b32 v251, s5, 17
	s_lshr_b32 s5, s2, 8
	s_and_b32 s0, s0, 0x1c0
	s_lshl_b32 s1, s1, 1
	s_lshl_b32 s10, s5, 9
	v_writelane_b32 v251, s10, 18
	s_add_u32 s10, s62, 0x380d8000
	s_addc_u32 s11, s63, 0
	v_writelane_b32 v251, s10, 19
	s_nop 1
	v_writelane_b32 v251, s11, 20
	s_add_u32 s10, s62, 0x2bcd8000
	s_addc_u32 s11, s63, 0
	v_writelane_b32 v251, s9, 21
	s_add_i32 s9, s9, 0x8800
	s_add_u32 s14, s62, 0x88000
	s_addc_u32 s15, s63, 0
	s_lshl_b32 s12, s0, 2
	v_writelane_b32 v251, s9, 22
	s_add_u32 s9, s14, s12
	v_writelane_b32 v251, s9, 23
	v_writelane_b32 v251, s14, 24
	s_addc_u32 s9, s15, 0
	s_add_i32 s1, s1, s5
	v_writelane_b32 v251, s15, 25
	v_writelane_b32 v251, s9, 26
	s_lshl_b32 s9, s89, 7
	s_and_b32 s13, s9, 0xffffff00
	s_lshl_b32 s9, s0, 1
	s_add_u32 s14, s82, s9
	s_addc_u32 s15, s83, 0
	s_cmpk_gt_u32 s2, 0xff
	v_writelane_b32 v251, s14, 27
	s_cselect_b64 s[34:35], -1, 0
	s_nop 0
	v_writelane_b32 v251, s15, 28
	s_and_b64 s[14:15], s[34:35], exec
	s_cselect_b32 s15, s10, s26
	s_cselect_b32 s14, s11, s27
	s_cselect_b32 s25, s16, 0x800
	s_add_u32 s28, s15, s12
	v_writelane_b32 v251, s25, 29
	s_addc_u32 s29, s14, 0
	v_writelane_b32 v251, s28, 30
	s_and_b32 s14, s23, 0x7fffff80
	s_add_i32 s13, s14, s13
	v_writelane_b32 v251, s29, 31
	v_writelane_b32 v251, s23, 32
	v_writelane_b32 v251, s13, 33
	s_and_b32 s13, s89, 0x1fffffe
	v_writelane_b32 v251, s13, 34
	s_add_u32 s14, s26, s12
	v_writelane_b32 v251, s26, 35
	s_addc_u32 s15, s27, 0
	s_add_u32 s10, s10, s12
	v_writelane_b32 v251, s27, 36
	v_writelane_b32 v251, s14, 37
	s_addc_u32 s11, s11, 0
	s_cmpk_lt_i32 s24, 0x1000
	v_writelane_b32 v251, s15, 38
	v_writelane_b32 v251, s10, 39
	s_mov_b32 s29, s65
	v_readlane_b32 s14, v250, 2
	v_writelane_b32 v251, s11, 40
	s_cselect_b64 s[10:11], -1, 0
	v_writelane_b32 v251, s10, 41
	v_readlane_b32 s15, v250, 3
	s_nop 0
	v_writelane_b32 v251, s11, 42
	s_bfe_u32 s10, s2, 0x10006
	s_lshl_b32 s11, s10, 9
	s_bitcmp1_b32 s2, 6
	v_writelane_b32 v251, s11, 43
	s_cselect_b64 s[12:13], -1, 0
	v_writelane_b32 v251, s12, 44
	s_cmp_eq_u32 s10, 0
	s_cselect_b64 s[36:37], -1, 0
	v_writelane_b32 v251, s13, 45
	v_writelane_b32 v251, s10, 46
	s_and_b64 s[10:11], s[36:37], exec
	s_cselect_b32 s10, 0x800, s16
	s_add_u32 s23, s62, 0x257d8000
	v_writelane_b32 v251, s10, 47
	s_addc_u32 s10, s63, 0
	s_cmpk_lt_i32 s89, 0x100
	v_writelane_b32 v251, s10, 48
	s_cselect_b64 s[10:11], -1, 0
	v_writelane_b32 v251, s10, 49
	s_nop 1
	v_writelane_b32 v251, s11, 50
	s_add_u32 s10, s62, 0x33ed8000
	s_addc_u32 s11, s63, 0
	v_writelane_b32 v251, s10, 51
	s_nop 1
	v_writelane_b32 v251, s11, 52
	s_lshl_b32 s10, s3, 9
	v_writelane_b32 v251, s10, 53
	s_add_u32 s10, s62, 0x146b8000
	s_addc_u32 s11, s63, 0
	v_writelane_b32 v251, s10, 54
	s_cmpk_lt_i32 s89, 0x3410
	s_nop 0
	v_writelane_b32 v251, s11, 55
	s_cselect_b64 s[10:11], -1, 0
	v_writelane_b32 v251, s10, 56
	s_nop 1
	v_writelane_b32 v251, s11, 57
	s_add_u32 s10, s62, 0x14eb8000
	s_addc_u32 s11, s63, 0
	v_writelane_b32 v251, s10, 58
	s_nop 1
	v_writelane_b32 v251, s11, 59
	s_add_u32 s10, s62, 0x150b8000
	s_addc_u32 s11, s63, 0
	v_writelane_b32 v251, s10, 60
	s_nop 1
	v_writelane_b32 v251, s11, 61
	s_add_u32 s10, s62, 0x150d8000
	v_writelane_b32 v251, s10, 62
	s_addc_u32 s10, s63, 0
	v_writelane_b32 v251, s10, 63
	s_add_u32 s10, s62, 0x191d8000
	v_writelane_b32 v252, s10, 0
	s_addc_u32 s10, s63, 0
	v_writelane_b32 v252, s10, 1
	s_add_u32 s10, s62, 0x1b258000
	v_writelane_b32 v252, s10, 2
	s_addc_u32 s10, s63, 0
	s_cmp_lt_i32 s24, 0x8400
	v_writelane_b32 v252, s10, 3
	s_cselect_b64 s[10:11], -1, 0
	v_writelane_b32 v252, s10, 4
	s_cmpk_lt_i32 s24, 0x800
	s_nop 0
	v_writelane_b32 v252, s11, 5
	s_cselect_b64 s[10:11], -1, 0
	s_ashr_i32 s12, s89, 3
	s_ashr_i32 s13, s3, 3
	s_and_b32 s38, s89, 7
	s_add_u32 s70, s62, 0x208000
	v_writelane_b32 v252, s10, 6
	s_addc_u32 s71, s63, 0
	s_nop 0
	v_writelane_b32 v252, s11, 7
	s_add_u32 s10, s62, 0x418000
	s_addc_u32 s11, s63, 0
	v_writelane_b32 v252, s10, 8
	s_nop 1
	v_writelane_b32 v252, s11, 9
	s_add_u32 s10, s62, 0x4000
	v_writelane_b32 v252, s10, 10
	s_addc_u32 s10, s63, 0
	v_writelane_b32 v252, s10, 11
	s_add_u32 s10, s62, 0x100000
	s_addc_u32 s11, s63, 0
	v_writelane_b32 v252, s10, 12
	s_nop 1
	v_writelane_b32 v252, s11, 13
	s_add_u32 s10, s62, 0x310000
	s_addc_u32 s11, s63, 0
	s_add_u32 s26, s62, 0x8a000
	v_writelane_b32 v252, s10, 14
	s_addc_u32 s27, s63, 0
	s_lshl_b32 s28, s75, 7
	v_writelane_b32 v252, s11, 15
	s_lshl_b64 s[10:11], s[28:29], 2
	s_add_u32 s10, s14, s10
	s_addc_u32 s11, s15, s11
	v_writelane_b32 v252, s10, 16
	s_nop 1
	v_writelane_b32 v252, s11, 17
	s_add_u32 s10, s62, 0xcc000
	v_writelane_b32 v252, s10, 18
	s_addc_u32 s10, s63, 0
	v_writelane_b32 v252, s10, 19
	s_mul_i32 s10, s75, 0xffffef80
	v_writelane_b32 v252, s17, 20
	s_add_i32 s10, s17, s10
	v_writelane_b32 v252, s10, 21
	s_cmp_lt_u32 s2, 64
	v_writelane_b32 v252, s13, 22
	s_cselect_b64 s[16:17], -1, 0
	v_writelane_b32 v252, s16, 23
	s_mul_i32 s10, s13, s38
	s_and_b32 s13, s3, 7
	v_writelane_b32 v252, s17, 24
	v_writelane_b32 v252, s12, 25
	s_add_i32 s12, s10, s12
	s_or_b32 s10, s28, 32
	v_writelane_b32 v252, s10, 26
	s_or_b32 s10, s28, 64
	v_writelane_b32 v252, s10, 27
; __device__ __forceinline__ Frame fresh(const Frame& F0) { Frame F = F0; int ln = lane_id_(); asm volatile("" : "+v"(ln)); F.lane = ln; F.tid = F0.wave * 64 + ln; return F; }
; #define SEAM(k) do { if (IN(k) && IN((k) + 1)) { xcd_barrier(bar); if (REPM & 1) xcd_barrier(bar); } } while (0)
; __global__ void __launch_bounds__(512, 2) mk_fwd(Args args) {
;     ...
;     for (int l = 0; l < 4; ++l) {
;         const int pb = 2 + l * 10, j = l >> 1; const bool even = (l & 1) == 0;
;         float* mods_l = F.mods + (size_t)l * 5 * 6144;
;         F.WB = args.ws + OFF_WB + (size_t)(l & 1) * WB_END;
;         if ((PHM & 4) && IN(pb + 0) && !(l & 1)) { for (int rep = 0; rep < ((REPM & 4) ? 2 : 1); ++rep) { ph_convert(fresh(F), l); __syncthreads(); } }
;         if (!(l & 1)) SEAM(pb + 0);
;         if ((PHM & 8) && IN(pb + 1)) {
;             const int N = even ? 4096 : 2048;
;             pg8::StaticOrder S; S.init(F.HB, F.WB + WB_IN, TT, N, 1024, F.G, F.wg);
;             S.lim = S.nwg;
;             pg8::EpiStoreBf16 E{(bf16_t*)(F.R1 + R1_P), N};
;             for (int rep = 0; rep < ((REPM & 8) ? 2 : 1); ++rep) pg8::gemm_phase(F.lds, 1024, S, E, F.wave);
;         } SEAM(pb + 1);
;         if (IN(pb + 2)) { if (even) { if (F.wg < 8 && F.G > 16) { ph_hg_ctx(fresh(F), j); } else if (PHM & 16) for (int rep = 0; rep < ((REPM & 16) ? 2 : 1); ++rep) { Frame Fa = fresh(F); if (F.G > 16) { Fa.wg = F.wg - 8; Fa.G = F.G - 8; } ph_attn(Fa, j); } if (PHM & 32) for (int rep = 0; rep < ((REPM & 32) ? 2 : 1); ++rep) ph_hg_a(fresh(F), j); } else { if (PHM & 64) for (int rep = 0; rep < ((REPM & 64) ? 2 : 1); ++rep) ph_lru_a(fresh(F), j); } } SEAM(pb + 2);
;         if (IN(pb + 3)) { if (even) { if (PHM & 128) for (int rep = 0; rep < ((REPM & 128) ? 2 : 1); ++rep) { ph_hg_b(fresh(F));
;                 { Frame Fc = fresh(F); Fc.WB = args.ws + OFF_WB + (size_t)((l + 1) & 1) * WB_END; ph_convert(Fc, l + 1); } } } else { if (PHM & 256) for (int rep = 0; rep < ((REPM & 256) ? 2 : 1); ++rep) ph_lru_b(fresh(F)); } } SEAM(pb + 3);
;         if (IN(pb + 4)) { if (even) { if (PHM & 512) for (int rep = 0; rep < ((REPM & 512) ? 2 : 1); ++rep) ph_hg_c(fresh(F), j); } else { if (PHM & 1024) for (int rep = 0; rep < ((REPM & 1024) ? 2 : 1); ++rep) ph_lru_c(fresh(F)); } } SEAM(pb + 4);
	s_mov_b32 s10, s28
	v_writelane_b32 v252, s10, 28
	s_nop 1
	v_writelane_b32 v252, s11, 29
	s_or_b32 s10, s28, 0x60
	v_writelane_b32 v252, s10, 30
	s_lshl_b32 s10, s75, 1
	v_writelane_b32 v252, s10, 31
	s_sub_i32 s10, s3, s89
	v_writelane_b32 v252, s10, 32
	s_add_u32 s10, s62, 0x9898080
	s_addc_u32 s11, s63, 0
	v_writelane_b32 v252, s10, 33
	s_nop 1
	v_writelane_b32 v252, s11, 34
	s_add_u32 s10, s62, 0x22e58000
	s_addc_u32 s11, s63, 0
	v_writelane_b32 v252, s10, 35
	s_lshl_b32 s16, s24, 3
	s_nop 0
	v_writelane_b32 v252, s11, 36
	s_add_i32 s10, s24, s80
	s_cmp_lt_i32 s10, 0x8400
	s_cselect_b64 s[28:29], -1, 0
	v_writelane_b32 v252, s28, 37
	s_lshl_b32 s10, s10, 3
	s_ashr_i32 s25, s24, 31
	v_writelane_b32 v252, s29, 38
	v_writelane_b32 v252, s10, 39
	s_lshl_b64 s[10:11], s[24:25], 12
	s_add_u32 s28, s14, s10
	v_writelane_b32 v252, s10, 40
	s_addc_u32 s29, s15, s11
	s_nop 0
	v_writelane_b32 v252, s11, 41
	s_lshl_b64 s[10:11], s[24:25], 3
	v_writelane_b32 v252, s28, 42
	s_add_u32 s10, s26, s10
	s_addc_u32 s11, s27, s11
	v_writelane_b32 v252, s29, 43
	v_writelane_b32 v252, s10, 44
	s_nop 1
	v_writelane_b32 v252, s11, 45
	s_add_i32 s10, s24, s81
	s_cmp_lt_i32 s10, 0x8400
	s_cselect_b64 s[10:11], -1, 0
	v_writelane_b32 v252, s10, 46
	s_nop 1
	v_writelane_b32 v252, s11, 47
	s_add_u32 s10, s62, 0x6a000
	s_addc_u32 s11, s63, 0
	v_writelane_b32 v252, s10, 48
	s_nop 1
	v_writelane_b32 v252, s11, 49
	s_add_u32 s10, s62, 0x70000
	s_addc_u32 s11, s63, 0
	v_writelane_b32 v252, s10, 50
	s_nop 1
	v_writelane_b32 v252, s11, 51
	s_add_u32 s10, s62, 0x76000
	s_addc_u32 s11, s63, 0
	v_writelane_b32 v252, s10, 52
	s_nop 1
	v_writelane_b32 v252, s11, 53
	s_add_u32 s10, s62, 0x7c000
	s_addc_u32 s11, s63, 0
	v_writelane_b32 v252, s10, 54
	s_nop 1
	v_writelane_b32 v252, s11, 55
	s_add_u32 s10, s62, 0x82000
	s_addc_u32 s11, s63, 0
	v_writelane_b32 v252, s10, 56
	s_add_i32 s28, s24, 0x400
	s_nop 0
	v_writelane_b32 v252, s11, 57
	s_lshl_b32 s10, s28, 3
	v_writelane_b32 v252, s10, 58
	s_add_i32 s10, s28, s80
	s_cmp_lt_i32 s10, 0x8400
	s_cselect_b64 s[30:31], -1, 0
	v_writelane_b32 v252, s30, 59
	s_lshl_b32 s10, s10, 3
	s_ashr_i32 s29, s28, 31
	v_writelane_b32 v252, s31, 60
	v_writelane_b32 v252, s10, 61
	s_lshl_b64 s[10:11], s[28:29], 12
	s_add_u32 s10, s14, s10
	s_addc_u32 s11, s15, s11
	v_writelane_b32 v252, s10, 62
	s_nop 1
	v_writelane_b32 v252, s11, 63
	s_lshl_b64 s[10:11], s[28:29], 3
	s_add_u32 s10, s26, s10
	v_writelane_b32 v253, s26, 0
	s_addc_u32 s11, s27, s11
	s_nop 0
	v_writelane_b32 v253, s27, 1
	v_writelane_b32 v253, s10, 2
	s_nop 1
	v_writelane_b32 v253, s11, 3
	s_add_i32 s10, s28, s81
	s_cmp_lt_i32 s10, 0x8400
	s_cselect_b64 s[10:11], -1, 0
	s_cmp_eq_u32 s8, 0
	v_writelane_b32 v253, s10, 4
	s_cselect_b32 s6, s7, s6
	s_cmpk_lt_i32 s6, 0x420
	v_writelane_b32 v253, s11, 5
	v_writelane_b32 v253, s6, 6
	s_cselect_b64 s[6:7], -1, 0
	v_writelane_b32 v253, s6, 7
	s_nop 1
	v_writelane_b32 v253, s7, 8
	s_or_b32 s6, s21, 0x400
	s_cmp_eq_u32 s13, 0
	v_writelane_b32 v253, s21, 9
	s_cselect_b32 s10, s12, s89
	v_writelane_b32 v253, s6, 10
	s_lshr_b32 s6, s10, 31
	s_add_i32 s6, s10, s6
	s_ashr_i32 s7, s6, 1
	v_writelane_b32 v253, s7, 11
	s_ashr_i32 s7, s10, 31
	s_lshr_b32 s7, s7, 30
	s_add_i32 s7, s10, s7
	s_and_b32 s6, s6, -2
	s_and_b32 s8, s7, -4
	s_ashr_i32 s12, s7, 2
	s_sub_i32 s14, s10, s8
	v_writelane_b32 v253, s10, 12
	s_sub_i32 s10, s10, s6
	s_mov_b32 s6, s12
	v_writelane_b32 v253, s6, 13
	s_mov_b32 s8, s14
	s_ashr_i32 s13, s12, 31
	v_writelane_b32 v253, s7, 14
	s_ashr_i32 s15, s14, 31
	v_writelane_b32 v253, s8, 15
	s_lshl_b64 s[6:7], s[12:13], 17
	s_lshl_b64 s[12:13], s[14:15], 17
	v_writelane_b32 v253, s9, 16
	v_writelane_b32 v253, s12, 17
	s_add_u32 s6, s82, s6
	s_addc_u32 s7, s83, s7
	v_writelane_b32 v253, s13, 18
	s_add_u32 s12, s6, 0x80
	v_writelane_b32 v253, s6, 19
	s_addc_u32 s13, s7, 0
	s_ashr_i32 s11, s10, 31
	v_writelane_b32 v253, s7, 20
	v_writelane_b32 v253, s12, 21
	s_mov_b32 s6, s10
	s_nop 0
	v_writelane_b32 v253, s13, 22
	v_writelane_b32 v253, s6, 23
	s_nop 1
	v_writelane_b32 v253, s7, 24
	s_lshl_b64 s[6:7], s[10:11], 19
	v_writelane_b32 v253, s6, 25
	s_nop 1
	v_writelane_b32 v253, s7, 26
	s_add_u32 s6, s76, s9
	s_addc_u32 s7, s77, 0
	v_writelane_b32 v253, s6, 27
	s_lshl_b32 s5, s5, 6
	s_sub_i32 s5, 0xc0, s5
	v_writelane_b32 v253, s7, 28
	s_abs_i32 s6, s3
	v_cvt_f32_u32_e32 v2, s6
	v_writelane_b32 v253, s6, 29
	s_sub_i32 s6, 0, s6
	s_and_b32 s2, s2, 0xffffff00
	v_rcp_iflag_f32_e32 v2, v2
	s_sub_i32 s2, 0, s2
	s_lshl_b32 s8, s3, 4
	s_ashr_i32 s9, s8, 31
	v_mul_f32_e32 v2, 0x4f7ffffe, v2
	v_cvt_u32_f32_e32 v2, v2
	s_nop 0
	v_readfirstlane_b32 s7, v2
	s_mul_i32 s6, s6, s7
	s_mul_hi_u32 s6, s7, s6
	s_add_i32 s6, s7, s6
	v_writelane_b32 v253, s6, 30
	s_lshl_b32 s6, s75, 8
	s_add_i32 s6, s6, 0
	s_add_i32 s7, s6, 0x11800
	v_writelane_b32 v253, s7, 31
	s_add_i32 s6, s6, 0x9000
	v_writelane_b32 v253, s6, 32
	v_writelane_b32 v253, s5, 33
	v_writelane_b32 v253, s2, 34
	s_add_i32 s2, s4, 0xffffebc0
	v_writelane_b32 v253, s2, 35
	s_add_i32 s2, s4, 0xfffff3c0
	v_writelane_b32 v253, s2, 36
; #define LAS __attribute__((address_space(3)))
; __device__ __forceinline__ const float* inp(const Frame& F, int i) {
;     const unsigned long long v = ((const LAS unsigned long long*)(F.lds + LDS_MISC + MISC_INP))[i];
;     const unsigned lo = (unsigned)__builtin_amdgcn_readfirstlane((int)(unsigned)v), hi = (unsigned)__builtin_amdgcn_readfirstlane((int)(unsigned)(v >> 32));
;     return (const float*)(((unsigned long long)hi << 32) | lo);
; }
; __global__ void __launch_bounds__(512, 2) mk_fwd(Args args) {
;     ...
;     volatile LAS unsigned* xbw = (volatile LAS unsigned*)(F.lds + LDS_MISC);
;     if (F.tid < 4) xbw[F.tid] = 0u;
;     if (F.tid < 30) ((LAS unsigned long long*)(F.lds + LDS_MISC + MISC_INP))[F.tid] = (unsigned long long)args.in[F.tid];
;     __syncthreads();
;     const int lo = args.ph_lo, hi = args.ph_hi;
;     XcdBarrier bar; bar.bar = (unsigned*)(args.ws + OFF_CTL); bar.x = 0; bar.st = xbw;
;     if (hi - lo > 1) bar = xcd_barrier_post((unsigned*)(args.ws + OFF_CTL), xbw);
	s_lshl_b32 s2, s89, 1
	s_add_i32 s4, s2, 0xfffff5e0
	v_writelane_b32 v253, s4, 37
	s_addk_i32 s2, 0xf9e0
	v_writelane_b32 v253, s2, 38
	s_add_i32 s2, s20, 0xffffd780
	v_writelane_b32 v253, s2, 39
	s_add_i32 s2, s20, 0xffffe780
	v_writelane_b32 v253, s2, 40
	s_lshl_b32 s2, s89, 11
	s_add_i32 s4, s2, 0xffd78000
	v_writelane_b32 v253, s4, 41
	s_add_i32 s2, s2, 0xffe78000
	v_writelane_b32 v253, s2, 42
	s_lshl_b32 s2, s89, 12
	s_add_i32 s4, s2, 0xfda70000
	v_writelane_b32 v253, s4, 43
	s_add_i32 s2, s2, 0xfdc70000
	v_writelane_b32 v253, s2, 44
	s_mov_b32 s2, s28
	v_writelane_b32 v253, s2, 45
	s_lshl_b32 s6, s3, 8
	s_lshl_b32 s96, s3, 7
	v_writelane_b32 v253, s3, 46
	s_lshl_b32 s2, s3, 5
	v_writelane_b32 v253, s2, 47
	s_add_i32 s2, s89, 0xfffffaf0
	v_writelane_b32 v253, s2, 48
	v_writelane_b32 v253, s6, 49
	s_lshl_b32 s6, s89, 4
	s_add_i32 s7, s6, 0xfffda700
	v_writelane_b32 v253, s7, 50
	s_lshl_b32 s7, s3, 6
	v_writelane_b32 v253, s7, 51
	s_lshl_b32 s7, s3, 13
	v_writelane_b32 v253, s7, 52
	s_lshl_b32 s7, s3, 14
	v_writelane_b32 v253, s7, 53
	s_lshl_b32 s7, s3, 12
	v_writelane_b32 v253, s7, 54
	s_lshl_b32 s7, s3, 11
	v_writelane_b32 v253, s7, 55
	s_lshl_b32 s7, s75, 9
	v_writelane_b32 v253, s7, 56
	s_add_i32 s7, s89, 0xfffffcf0
	s_lshl_b32 s2, s89, 6
	v_writelane_b32 v253, s7, 57
	v_writelane_b32 v253, s2, 58
	s_add_i32 s2, s2, 0xffff4000
	v_writelane_b32 v253, s2, 59
	s_add_i32 s2, s6, 0xfffdc700
	v_writelane_b32 v253, s2, 60
	s_lshl_b32 s2, s24, 6
	v_writelane_b32 v253, s2, 61
	s_add_i32 s2, s6, s8
	v_writelane_b32 v253, s2, 62
	s_add_i32 s2, s6, 0xfffffc00
	v_writelane_b32 v254, s2, 0
	s_add_i32 s2, s24, 0xfffffc00
	v_writelane_b32 v254, s2, 1
	v_writelane_b32 v254, s16, 2
	s_add_i32 s2, s16, 0x2000
	v_writelane_b32 v254, s2, 3
	s_add_i32 s2, s81, 0x400
	v_writelane_b32 v254, s2, 4
	s_mov_b32 s2, s24
	v_writelane_b32 v254, s2, 5
	v_writelane_b32 v253, s6, 63
	s_lshl_b64 s[6:7], s[24:25], 11
	v_writelane_b32 v254, s3, 6
	v_writelane_b32 v254, s6, 7
	s_add_i32 s4, s28, s8
	s_ashr_i32 s5, s4, 31
	v_writelane_b32 v254, s7, 8
	s_lshl_b64 s[6:7], s[8:9], 11
	v_writelane_b32 v254, s6, 9
	s_mul_hi_i32 s2, s1, 0x42
	s_mulk_i32 s1, 0x42
	v_writelane_b32 v254, s7, 10
	s_lshl_b64 s[6:7], s[8:9], 12
	v_writelane_b32 v254, s6, 11
	v_mov_b32_e32 v2, 0
	s_nop 0
	v_writelane_b32 v254, s7, 12
	s_lshl_b64 s[6:7], s[4:5], 3
	s_add_u32 s6, s6, 0x8a000
	s_addc_u32 s7, s7, 0
	v_writelane_b32 v254, s6, 13
	s_lshl_b64 s[4:5], s[4:5], 12
	s_lshl_b32 s12, s0, 1
	v_writelane_b32 v254, s7, 14
	v_writelane_b32 v254, s2, 15
	v_writelane_b32 v254, s1, 16
	v_writelane_b32 v254, s4, 17
	s_add_i32 s1, 0, 0x209e8
	s_add_i32 s0, 0, 0x20990
	v_writelane_b32 v254, s5, 18
	v_writelane_b32 v254, s1, 19
	s_add_i32 s1, 0, 0x209d0
	v_writelane_b32 v254, s1, 20
	s_add_i32 s1, 0, 0x209e0
	v_writelane_b32 v254, s1, 21
	s_add_i32 s1, 0, 0x209d8
	v_writelane_b32 v254, s1, 22
	s_add_i32 s1, 0, 0x209c8
	v_writelane_b32 v254, s1, 23
	s_add_i32 s1, 0, 0x209c0
	v_writelane_b32 v254, s1, 24
	s_add_i32 s1, 0, 0x209b0
	v_writelane_b32 v254, s1, 25
	s_add_i32 s1, 0, 0x20948
	v_writelane_b32 v254, s1, 26
	s_add_i32 s1, 0, 0x20940
	v_writelane_b32 v254, s1, 27
	s_add_i32 s1, 0, 0x20000
	v_writelane_b32 v254, s1, 28
	s_add_i32 s1, 0, 0x20004
	v_writelane_b32 v254, s1, 29
	s_add_i32 s1, 0, 0x20970
	v_writelane_b32 v254, s1, 30
	s_add_i32 s1, 0, 0x20988
	v_writelane_b32 v254, s1, 31
	s_add_i32 s1, 0, 0x20998
	v_writelane_b32 v254, s1, 32
	s_add_i32 s1, 0, 0x11c00
	v_writelane_b32 v254, s1, 33
	s_add_i32 s1, 0, 0x11d00
	v_writelane_b32 v254, s1, 34
	s_add_i32 s1, 0, 0x11e00
	v_writelane_b32 v254, s1, 35
	s_add_i32 s1, 0, 0x11f00
	v_writelane_b32 v254, s1, 36
	s_add_i32 s1, 0, 0x12100
	v_writelane_b32 v254, s1, 37
	s_add_i32 s1, 0, 0x12200
	v_writelane_b32 v254, s1, 38
	s_add_i32 s1, 0, 0x20950
	v_writelane_b32 v254, s1, 39
	s_add_i32 s1, 0, 0x20960
	v_writelane_b32 v254, s1, 40
	v_writelane_b32 v254, s0, 41
	s_add_i32 s0, 0, 0x20980
	v_writelane_b32 v254, s0, 42
	s_add_i32 s0, 0, 0x209a8
	v_writelane_b32 v254, s0, 43
	s_add_i32 s0, 0, 0x20968
	v_writelane_b32 v254, s0, 44
	s_add_i32 s0, 0, 0x209b8
	v_writelane_b32 v254, s0, 45
	s_add_i32 s0, 0, 0x20140
	v_writelane_b32 v254, s0, 46
	s_add_i32 s0, 0, 0x20048
	v_writelane_b32 v254, s0, 47
	s_add_i32 s0, 0, 0x20254
	v_writelane_b32 v254, s0, 48
	s_add_i32 s0, 0, 0x201d0
	v_writelane_b32 v254, s0, 49
	s_add_i32 s0, 0, 0x20930
	v_writelane_b32 v254, s0, 50
	s_add_i32 s0, 0, 0x20250
	v_writelane_b32 v254, s0, 51
	v_cmp_eq_u32_e64 s[0:1], 0, v0
	s_nop 1
	v_writelane_b32 v254, s0, 52
	s_nop 1
	v_writelane_b32 v254, s1, 53
	s_mov_b32 s0, s8
	v_writelane_b32 v254, s0, 54
	s_nop 1
	v_writelane_b32 v254, s1, 55
	s_lshl_b64 s[0:1], s[8:9], 3
	v_writelane_b32 v254, s0, 56
	s_nop 1
	v_writelane_b32 v254, s1, 57
	v_writelane_b32 v254, s40, 58
	s_mov_b32 s0, s65
	s_nop 0
	v_writelane_b32 v254, s41, 59
	v_writelane_b32 v254, s75, 60
	v_writelane_b32 v254, s79, 61
	v_writelane_b32 v254, s38, 62
	v_writelane_b32 v254, s70, 63
	s_nop 1
	v_writelane_b32 v255, s71, 0
	s_branch .LBB0_92

; #define LAS __attribute__((address_space(3)))
; __device__ __forceinline__ void ph_lru_a(const Frame& F, int jj) {
;     ...
;     for (int task = F.wg; task < NTASK; task += F.G) {
;         const int grp = task % 11, kb = (task / 11) & 15, b = task / (11 * 16);
;         __syncthreads();
;         for (int i = F.tid; i < 4 * 4096 / 8; i += 512) { const int mg = i >> 9, r = i & 511;
;             *(LAS u32x4*)(Wl + (mg * 64 + (r >> 3)) * 72 + (r & 7) * 8) = *(const u32x4*)(wsrc + ((size_t)mg * 16 + kb) * 4096 + r * 8); }
;         for (int i = F.tid; i < 11 * 64; i += 512) { const int kind = i >> 6, ch = kb * 64 + (i & 63); float v;
;             if (kind < 4) v = cw[kind * 1024 + ch]; else if (kind == 4) v = cb[ch];
;             else { const int d = (kind - 5) / 3, w = (kind - 5) % 3; v = (w == 0) ? b_a[d * 1024 + ch] : (w == 1) ? b_x[d * 1024 + ch] : -8.0f * log1pf(__expf(-lam[d * 1024 + ch])); }
;             CT[i] = v; }
;         __syncthreads();
;         const int nt0 = grp * 48;
;         LruRaw raw; lru_load(F, b, kb, nt0 + F.wave, raw);
.LBB0_434:
	v_cndmask_b32_e64 v0, 0, 1, s[86:87]
	s_andn2_b64 vcc, exec, s[0:1]
	v_cmp_ne_u32_e64 s[40:41], 1, v0
	s_cbranch_vccnz .LBB0_749
	s_and_b64 vcc, exec, s[40:41]
	s_mov_b64 s[0:1], -1
	s_cbranch_vccnz .LBB0_473
	v_readlane_b32 s0, v254, 30
	s_waitcnt vmcnt(0)
	v_mov_b32_e32 v4, v177
	v_readlane_b32 s5, v254, 31
	v_mov_b32_e32 v0, s0
	ds_read_b128 v[6:9], v0
	v_mov_b32_e32 v0, s5
	ds_read_b64 v[0:1], v0
	v_readlane_b32 s7, v254, 32
	v_readlane_b32 s14, v251, 6
	s_waitcnt lgkmcnt(0)
	v_readfirstlane_b32 s1, v7
	v_readfirstlane_b32 s4, v6
	v_readfirstlane_b32 s6, v0
	v_mov_b32_e32 v0, s7
	v_readfirstlane_b32 s0, v9
	v_readfirstlane_b32 s2, v8
	ds_read2_b64 v[6:9], v0 offset1:1
	v_readlane_b32 s15, v251, 7
	s_mov_b32 s22, s26
	v_readfirstlane_b32 s5, v1
	s_and_b64 vcc, exec, s[14:15]
	s_waitcnt lgkmcnt(0)
	v_readfirstlane_b32 s8, v7
	v_readfirstlane_b32 s10, v6
	v_readfirstlane_b32 s7, v9
	v_readfirstlane_b32 s9, v8
	s_cbranch_vccz .LBB0_472
	s_mov_b32 s14, s22
	s_mov_b32 s15, s65
	s_lshl_b64 s[16:17], s[14:15], 14
	s_lshl_b64 s[20:21], s[14:15], 12
	s_add_u32 s52, s4, s16
	s_addc_u32 s53, s1, s17
	s_add_u32 s58, s2, s20
	s_addc_u32 s59, s0, s21
	s_lshl_b64 s[16:17], s[14:15], 13
	s_add_u32 s66, s6, s16
	s_addc_u32 s67, s5, s17
	s_add_u32 s0, s10, s16
	v_add_u32_e32 v3, s79, v4
	s_addc_u32 s1, s8, s17
	s_movk_i32 s2, 0x800
	s_add_u32 s4, s9, s16
	v_cmp_gt_i32_e64 s[42:43], s2, v3
	s_movk_i32 s2, 0x2c0
	v_and_b32_e32 v5, 0x1ff, v3
	v_and_b32_e32 v94, -16, v4
	s_addc_u32 s5, s7, s17
	v_cmp_gt_i32_e64 s[44:45], s2, v3
	v_lshlrev_b32_e32 v6, 4, v5
	v_readlane_b32 s6, v255, 4
	v_lshlrev_b32_e32 v5, 2, v94
	v_readlane_b32 s2, v254, 33
	v_mov_b32_e32 v7, v2
	v_readlane_b32 s7, v255, 5
	v_add_u32_e32 v107, s2, v5
	s_add_i32 s2, 0, 0x11800
	v_lshl_add_u64 v[6:7], s[6:7], 0, v[6:7]
	s_mov_b64 s[6:7], 0x6ba0000
	v_add_u32_e32 v108, s2, v5
	v_readlane_b32 s2, v252, 20
	v_and_b32_e32 v104, 15, v4
	v_lshl_add_u64 v[92:93], v[6:7], 0, s[6:7]
	v_mov_b32_e32 v6, s2
	s_movk_i32 s2, 0x110
	v_mad_u32_u24 v6, v104, s2, v6
	v_readlane_b32 s2, v254, 34
	v_add_u32_e32 v109, v6, v5
	v_lshlrev_b32_e32 v5, 1, v4
	v_add_u32_e32 v111, s2, v94
	v_readlane_b32 s2, v254, 35
	v_ashrrev_i32_e32 v0, 2, v4
	v_and_b32_e32 v5, 0xffffffe0, v5
	v_add_u32_e32 v112, s2, v94
	v_readlane_b32 s2, v254, 36
	v_and_b32_e32 v0, -4, v0
	v_ashrrev_i32_e32 v95, 31, v94
	v_add_u32_e32 v113, s2, v94
	s_add_i32 s2, 0, 0x12000
	v_add_u32_e32 v115, s2, v94
	v_readlane_b32 s2, v254, 37
	v_add_u32_e32 v110, v6, v5
	v_sub_u32_e32 v5, 0, v94
	v_add_u32_e32 v116, s2, v94
	v_readlane_b32 s2, v254, 38
	v_mul_u32_u24_e32 v6, 0x90, v104
	v_ashrrev_i32_e32 v1, 31, v0
	v_add_u32_e32 v117, s2, v94
	v_readlane_b32 s2, v253, 56
	v_bfe_u32 v105, v3, 3, 6
	v_and_b32_e32 v106, 63, v4
	v_lshl_add_u32 v118, v4, 3, s2
	v_readlane_b32 s2, v253, 31
	v_add3_u32 v114, 0, v6, v94
	v_lshl_add_u64 v[96:97], v[94:95], 1, s[82:83]
	v_lshl_add_u32 v119, v4, 2, s2
	v_add_u32_e32 v120, v110, v5
	s_movk_i32 s101, 0x2bf
	s_cmpk_eq_i32 s3, 0x100
	s_cselect_b32 s32, 1, 0
	s_cselect_b32 s100, 0x7b, 39
	s_cselect_b32 s101, 0xff, s101
	s_mov_b32 s11, s89
	s_branch .LBB0_439
.LBB0_438:
	s_add_i32 s11, s11, s3
	s_cmp_gt_i32 s11, s101
	s_cbranch_scc1 .LBB0_472
.LBB0_439:
	s_mul_hi_i32 s13, s11, 0x2e8ba2e9
	s_lshr_b32 s16, s13, 31
	s_ashr_i32 s10, s13, 1
	s_add_i32 s10, s10, s16
	s_lshr_b32 s14, s11, 2
	s_cmp_lg_u32 s32, 0
	s_cselect_b32 s10, s14, s10
	s_and_b32 s2, s10, 15
	s_waitcnt vmcnt(0)
	s_barrier
	s_and_saveexec_b64 s[6:7], s[42:43]
	s_movk_i32 s14, 0x90
	s_cbranch_execz .LBB0_442
	s_lshl_b32 s64, s2, 13
	v_lshl_add_u64 v[4:5], v[92:93], 0, s[64:65]
	s_mov_b64 s[8:9], 0x20000
	global_load_dwordx4 v[210:213], v[4:5], off
	v_lshl_add_u64 v[226:227], v[4:5], 0, s[8:9]
	global_load_dwordx4 v[214:217], v[226:227], off
	v_lshl_add_u64 v[226:227], v[226:227], 0, s[8:9]
	global_load_dwordx4 v[218:221], v[226:227], off
	v_lshl_add_u64 v[226:227], v[226:227], 0, s[8:9]
	global_load_dwordx4 v[222:225], v[226:227], off
	v_and_b32_e32 v13, 56, v118
	s_movk_i32 s17, 0x5ff
	v_lshlrev_b32_e32 v13, 1, v13
	v_mul_lo_u32 v12, v105, s14
	v_add3_u32 v12, 0, v12, v13
	s_waitcnt vmcnt(0)
	ds_write_b128 v12, v[210:213]
	ds_write_b128 v12, v[214:217] offset:9216
	ds_write_b128 v12, v[218:221] offset:18432
	ds_write_b128 v12, v[222:225] offset:27648

; __device__ __forceinline__ void lru_load(const Frame& F, int b, int kb, int nt, LruRaw& R) {
;     const bf16_t* P = (const bf16_t*)(F.R1 + R1_P);
;     const int tk = F.lane & 15, g = F.lane >> 4;
;     const int len = nt < 16 ? CTXL : SEQ, tpos = (nt < 16 ? nt * 16 : (nt - 16) * 16) + tk;
;     const bf16_t* pbase = P + (size_t)((nt < 16 ? b * CTXL : TC + b * SEQ)) * 2048 + 1024 + kb * 64 + g * 16;
;     unsigned okm = 0u;
; #pragma unroll
;     for (int tap = 0; tap < 4; ++tap) { const int tp = tpos + tap - 2; const bool ok = (tp >= 0 && tp < len); const bf16_t* pr = pbase + (size_t)(ok ? tp : tpos) * 2048;
;         okm |= ok ? (1u << tap) : 0u;
;         R.a[tap] = *(const u32x4*)pr; R.b[tap] = *(const u32x4*)(pr + 8); }
;     R.ok = okm;
; __device__ __forceinline__ void ph_lru_a(const Frame& F, int jj) {
;     ...
;         const int nt0 = grp * 48;
;         LruRaw raw; lru_load(F, b, kb, nt0 + F.wave, raw);
;         for (int ti = F.wave; ti < 48; ti += 8) {
;             const int nt = nt0 + ti;
;             float av[2][4][4], xv[2][4][4]; unsigned pw[2][4][4];
;             lru_conv(F, raw, CT, ucb);
;             lru_load(F, b, kb, nt0 + min(ti + 8, 40 + F.wave), raw);
;             lru_gates(F, Wl, CT, ucb, av, pw);
;             const int row = lru_row(b, nt, tk);
.LBB0_463:
	s_or_b64 exec, exec, s[6:7]
	v_readlane_b32 s6, v251, 8
	v_readlane_b32 s7, v251, 9
	s_andn2_b64 vcc, exec, s[6:7]
	s_waitcnt lgkmcnt(0)
	s_barrier
	s_cbranch_vccnz .LBB0_438
	s_mul_i32 s2, s10, 11
	s_sub_i32 s2, s11, s2
	s_mul_i32 s2, s2, 48
	s_and_b32 s6, s11, 3
	s_mulk_i32 s6, 0x84
	s_cmp_lg_u32 s32, 0
	s_cselect_b32 s2, s6, s2
	s_add_i32 s6, s2, s75
	s_lshl_b32 s7, s6, 4
	s_cmp_lt_i32 s6, 16
	s_cselect_b32 s17, 0x100, s88
	s_add_i32 s8, s7, 0xffffff00
	s_cmp_lt_i32 s6, 16
	s_cselect_b32 s20, s7, s8
	s_ashr_i32 s7, s13, 5
	s_add_i32 s21, s7, s16
	s_lshr_b32 s7, s11, 6
	s_cmp_lg_u32 s32, 0
	s_cselect_b32 s21, s7, s21
	s_lshl_b32 s24, s21, 13
	s_lshl_b32 s13, s21, 8
	s_or_b32 s16, s24, 0x400
	s_cmp_lt_i32 s6, 16
	s_cselect_b32 s6, s13, s16
	s_ashr_i32 s7, s6, 31
	s_lshl_b64 s[6:7], s[6:7], 12
	s_add_u32 s6, s82, s6
	v_or_b32_e32 v14, s20, v104
	s_addc_u32 s7, s83, s7
	s_lshl_b32 s8, s64, 1
	v_add_u32_e32 v4, 1, v14
	s_add_u32 s6, s6, s8
	v_cmp_lt_i32_e32 vcc, -2, v14
	v_cmp_gt_i32_e64 s[46:47], s17, v4
	s_addc_u32 s7, s7, 0
	s_and_b64 vcc, vcc, s[46:47]
	s_cmp_gt_i32 s20, -1
	v_lshl_add_u64 v[12:13], v[94:95], 1, s[6:7]
	s_cselect_b64 s[6:7], -1, 0
	v_cmp_gt_i32_e64 s[46:47], s17, v14
	s_and_b64 s[6:7], s[6:7], s[46:47]
	v_cmp_lt_i32_e64 s[46:47], 0, v14
	v_cmp_ge_i32_e64 s[48:49], s17, v14
	v_add_u32_e32 v26, -2, v14
	s_and_b64 s[46:47], s[46:47], s[48:49]
	v_cmp_lt_i32_e64 s[48:49], 1, v14
	v_cmp_gt_i32_e64 s[50:51], s17, v26
	v_cndmask_b32_e64 v15, 0, 4, s[6:7]
	v_cndmask_b32_e64 v16, 0, 2, s[46:47]
	s_and_b64 s[48:49], s[48:49], s[50:51]
	v_cndmask_b32_e32 v4, v14, v4, vcc
	v_or_b32_e32 v15, v15, v16
	v_cndmask_b32_e64 v16, 0, 1, s[48:49]
	v_cndmask_b32_e64 v17, 0, 8, vcc
	v_ashrrev_i32_e32 v5, 31, v4
	v_or3_b32 v36, v15, v16, v17
	v_ashrrev_i32_e32 v15, 31, v14
	v_lshlrev_b64 v[4:5], 12, v[4:5]
	v_lshlrev_b64 v[16:17], 12, v[14:15]
	v_lshl_add_u64 v[8:9], v[12:13], 0, v[4:5]
	v_lshl_add_u64 v[20:21], v[12:13], 0, v[16:17]
	global_load_dwordx4 v[4:7], v[8:9], off offset:2064
	s_nop 0
	global_load_dwordx4 v[8:11], v[8:9], off offset:2048
	s_nop 0
	global_load_dwordx4 v[16:19], v[20:21], off offset:2064
	global_load_dwordx4 v[28:31], v[20:21], off offset:2048
	v_subbrev_co_u32_e64 v20, vcc, 0, v14, s[46:47]
	v_ashrrev_i32_e32 v21, 31, v20
	v_cndmask_b32_e64 v14, v14, v26, s[48:49]
	v_lshlrev_b64 v[20:21], 12, v[20:21]
	v_ashrrev_i32_e32 v15, 31, v14
	v_lshl_add_u64 v[24:25], v[12:13], 0, v[20:21]
	v_lshlrev_b64 v[14:15], 12, v[14:15]
	global_load_dwordx4 v[20:23], v[24:25], off offset:2064
	global_load_dwordx4 v[32:35], v[24:25], off offset:2048
	v_lshl_add_u64 v[24:25], v[12:13], 0, v[14:15]
	global_load_dwordx4 v[12:15], v[24:25], off offset:2064
	s_nop 0
	global_load_dwordx4 v[24:27], v[24:25], off offset:2048
	s_mov_b32 s9, s65
	s_or_b32 s17, s24, 0x300
	s_lshl_b32 s6, s64, 2
	v_readlane_b32 s7, v251, 2
	s_add_u32 s6, s7, s6
	v_readlane_b32 s7, v251, 3
	v_lshl_add_u64 v[100:101], v[96:97], 0, s[8:9]
	s_mov_b32 s8, s2
	s_addc_u32 s7, s7, 0
	v_readlane_b32 s14, v251, 4
	s_add_i32 s8, s75, s8
	v_lshl_add_u64 v[38:39], s[64:65], 0, v[0:1]
	s_lshl_b32 s26, s21, 1
	v_readlane_b32 s15, v251, 5
	s_or_b32 s27, s26, 1
	v_lshl_add_u64 v[98:99], v[38:39], 2, s[14:15]
	v_lshl_or_b32 v121, s8, 4, v104
	s_mov_b32 s30, s75
	s_waitcnt vmcnt(0)
	s_branch .LBB0_466
.LBB0_465:
	s_or_b64 exec, exec, s[24:25]
	s_cmp_gt_i32 s54, -1
	s_cselect_b64 s[8:9], -1, 0
	v_cmp_gt_i32_e32 vcc, s31, v102
	s_and_b64 s[8:9], s[8:9], vcc
	v_cndmask_b32_e64 v37, 0, 2, s[48:49]
	v_cndmask_b32_e64 v38, 0, 4, s[8:9]
	v_cndmask_b32_e64 v36, 0, 1, s[46:47]
	v_or_b32_e32 v37, v38, v37
	v_cndmask_b32_e64 v38, 0, 8, s[50:51]
	v_or3_b32 v36, v37, v36, v38
	s_cmp_gt_u32 s28, s100
	v_add_u32_e32 v121, 0x80, v121
	s_cbranch_scc1 .LBB0_438
